# barrier waits convert with waves 1-5; P11 flush: only waves 1-2 fetch new batches (P13 remap kept)
# speedup vs baseline: 1.0077x; 1.0001x over previous
; __device__ __forceinline__ int lane_id_now() { unsigned z = 0u; asm volatile("" : "+v"(z)); return (int)__builtin_amdgcn_mbcnt_hi(~0u, __builtin_amdgcn_mbcnt_lo(~0u, z)); }
; __device__ __forceinline__ bool cv_one(const CvWork& w) {
;     if (w.wave == 0) return false;
;     int it = __builtin_amdgcn_readfirstlane(w.cur[2 * w.wave]); const int end = __builtin_amdgcn_readfirstlane(w.cur[2 * w.wave + 1]);
;     if (it >= end) {
;         if (it > CV_ITEMS) return false;
;         unsigned base = 0u; if (lane_id_now() == 0) base = __hip_atomic_fetch_add(w.q, (unsigned)CV_BATCH, __ATOMIC_RELAXED, __HIP_MEMORY_SCOPE_AGENT);
;         base = __builtin_amdgcn_readfirstlane(base);
;         if (base >= (unsigned)CV_ITEMS) { w.cur[2 * w.wave] = CV_ITEMS + 1; w.cur[2 * w.wave + 1] = 0; return false; }
;         it = (int)base; w.cur[2 * w.wave + 1] = (int)base + CV_BATCH;
;     }
.LBB0_1416:
	ds_read_b32 v0, v2
	ds_read_b32 v5, v2 offset:4
	s_waitcnt lgkmcnt(1)
	v_readfirstlane_b32 s28, v0
	s_waitcnt lgkmcnt(0)
	v_readfirstlane_b32 s4, v5
	s_cmp_lt_i32 s28, s4
	s_mov_b64 s[4:5], -1
	s_cbranch_scc1 .LBB0_1427
	s_cmp_gt_u32 s89, 2
	s_cbranch_scc1 .LBB0_1430
	s_cmp_lt_i32 s28, 0x10001
	s_mov_b64 s[6:7], 0
	s_cbranch_scc0 .LBB0_1428
	v_mov_b32_e32 v5, 0
	v_mov_b32_e32 v0, 0
	v_mbcnt_lo_u32_b32 v5, -1, v5
	v_mbcnt_hi_u32_b32 v5, -1, v5
	v_cmp_eq_u32_e32 vcc, 0, v5
	s_and_saveexec_b64 s[6:7], vcc
	s_cbranch_execz .LBB0_1422
	s_mov_b64 s[10:11], exec
	v_mbcnt_lo_u32_b32 v0, s10, 0
	v_mbcnt_hi_u32_b32 v0, s11, v0
	v_cmp_eq_u32_e32 vcc, 0, v0
	s_and_saveexec_b64 s[8:9], vcc
	s_cbranch_execz .LBB0_1421
	s_bcnt1_i32_b64 s10, s[10:11]
	s_lshl_b32 s10, s10, 2
	v_mov_b32_e32 v5, s10
	global_atomic_add v5, v1, v5, s[90:91] sc0
